# v22 + grid barrier XCD leader issues its acquire together with the release (before the top-level exchange)
# baseline (speedup 1.0000x reference)
; __device__ __forceinline__ unsigned xb_ld(unsigned* p)              { return __hip_atomic_load(p, __ATOMIC_RELAXED, __HIP_MEMORY_SCOPE_AGENT); }
; __device__ __forceinline__ unsigned xb_add(unsigned* p, unsigned v) { return __hip_atomic_fetch_add(p, v, __ATOMIC_RELAXED, __HIP_MEMORY_SCOPE_AGENT); }
; #define XB_SPIN(cond, bar) do { unsigned _sp = 0; while (cond) { __builtin_amdgcn_s_sleep(1); \
;     if ((++_sp & 255u) == 0u) { if (xb_ld(&(bar)[XB_TMO])) break; if (_sp > XB_SPIN_CAP) { atomicAdd(&(bar)[XB_TMO], 1u); break; } } } } while (0)
; __device__ __forceinline__ void xcd_barrier(const XcdBarrier& b) {
;     ...
;         if (old + 1u == (gen + 1u) * nloc) {
;             __builtin_amdgcn_fence(__ATOMIC_RELEASE, "agent");
;             asm volatile("s_waitcnt vmcnt(0)" ::: "memory");
;             const unsigned og = xb_add(&bar[XB_TOP], 1u);
;             const unsigned tg = og / nx;
;             if (og + 1u == (tg + 1u) * nx) xb_add(&bar[XB_TOPGEN], 1u);
;             else XB_SPIN(xb_ld(&bar[XB_TOPGEN]) == tg, bar);
;             __builtin_amdgcn_fence(__ATOMIC_ACQUIRE, "agent");
.LBB0_85:
	s_andn2_saveexec_b64 s[4:5], s[4:5]
	s_cbranch_execz .LBB0_101
	v_mov_b32_e32 v1, s38
	v_add_co_u32_e32 v4, vcc, 0x3000, v1
	v_mov_b32_e32 v1, s39
	buffer_wbl2 sc1
	buffer_inv sc1
	s_waitcnt vmcnt(0)
	v_addc_co_u32_e32 v5, vcc, 0, v1, vcc
	v_mov_b32_e32 v1, 1
	flat_atomic_add v1, v[4:5], v1 offset:1024 sc0
	v_cvt_f32_u32_e32 v3, v2
	v_sub_u32_e32 v4, 0, v2
	s_add_u32 s4, s38, 0x3500
	s_addc_u32 s5, s39, 0
	v_rcp_iflag_f32_e32 v3, v3
	s_mov_b64 s[8:9], -1
	v_mul_f32_e32 v3, 0x4f7ffffe, v3
	v_cvt_u32_f32_e32 v3, v3
	v_mul_lo_u32 v4, v4, v3
	v_mul_hi_u32 v4, v3, v4
	v_add_u32_e32 v3, v3, v4
	s_waitcnt vmcnt(0) lgkmcnt(0)
	v_mul_hi_u32 v3, v1, v3
	v_mul_lo_u32 v5, v3, v2
	v_add_u32_e32 v4, 1, v1
	v_sub_u32_e32 v1, v1, v5
	v_add_u32_e32 v6, 1, v3
	v_cmp_ge_u32_e32 vcc, v1, v2
	v_sub_u32_e32 v5, v1, v2
	s_nop 0
	v_cndmask_b32_e32 v3, v3, v6, vcc
	v_cndmask_b32_e32 v1, v1, v5, vcc
	v_add_u32_e32 v5, 1, v3
	v_cmp_ge_u32_e32 vcc, v1, v2
	s_nop 1
	v_cndmask_b32_e32 v1, v3, v5, vcc
	v_mad_u64_u32 v[2:3], s[6:7], v2, v1, v[2:3]
	v_cmp_ne_u32_e32 vcc, v4, v2
	v_mov_b64_e32 v[2:3], s[4:5]
	s_and_saveexec_b64 s[6:7], vcc
	s_cbranch_execz .LBB0_98
	v_mov_b64_e32 v[2:3], s[4:5]
	flat_load_dword v2, v[2:3] sc1
	s_mov_b64 s[12:13], 0
	s_waitcnt vmcnt(0) lgkmcnt(0)
	v_cmp_eq_u32_e32 vcc, v2, v1
	s_and_saveexec_b64 s[10:11], vcc
	s_cbranch_execz .LBB0_97
	s_add_u32 s8, s38, 0x200
	s_addc_u32 s9, s39, 0
	s_mov_b32 s3, 1
	s_branch .LBB0_90

; __device__ __forceinline__ unsigned xb_add(unsigned* p, unsigned v) { return __hip_atomic_fetch_add(p, v, __ATOMIC_RELAXED, __HIP_MEMORY_SCOPE_AGENT); }
; __device__ __forceinline__ void xcd_barrier(const XcdBarrier& b) {
;     ...
;             __builtin_amdgcn_fence(__ATOMIC_ACQUIRE, "agent");
;             xb_add(&bar[XB_XGEN(bx)], 1u);
.LBB0_100:
	s_or_b64 exec, exec, s[4:5]
	s_addk_i32 s2, 0x900
	s_mov_b32 s3, 0
	s_lshl_b64 s[2:3], s[2:3], 2
	s_add_u32 s2, s38, s2
	s_addc_u32 s3, s39, s3
	v_mov_b32_e32 v1, 1
	v_mov_b64_e32 v[2:3], s[2:3]
	s_waitcnt vmcnt(0) lgkmcnt(0)
	flat_atomic_add v[2:3], v1
	s_waitcnt vmcnt(0)

; __device__ __forceinline__ unsigned xb_add(unsigned* p, unsigned v) { return __hip_atomic_fetch_add(p, v, __ATOMIC_RELAXED, __HIP_MEMORY_SCOPE_AGENT); }
; __device__ __forceinline__ void xcd_barrier(const XcdBarrier& b) {
;     ...
;             __builtin_amdgcn_fence(__ATOMIC_ACQUIRE, "agent");
;             xb_add(&bar[XB_XGEN(bx)], 1u);
.LBB0_102:
	s_or_b64 exec, exec, s[4:5]
	s_add_i32 s66, s2, 0x900
	s_lshl_b64 s[4:5], s[66:67], 2
	s_add_u32 s4, s38, s4
	s_addc_u32 s5, s39, s5
	v_mov_b64_e32 v[2:3], s[4:5]
	s_waitcnt vmcnt(0) lgkmcnt(0)
	flat_atomic_add v[2:3], v238
	s_waitcnt vmcnt(0)

; __device__ __forceinline__ unsigned xb_ld(unsigned* p)              { return __hip_atomic_load(p, __ATOMIC_RELAXED, __HIP_MEMORY_SCOPE_AGENT); }
; __device__ __forceinline__ unsigned xb_add(unsigned* p, unsigned v) { return __hip_atomic_fetch_add(p, v, __ATOMIC_RELAXED, __HIP_MEMORY_SCOPE_AGENT); }
; #define XB_SPIN(cond, bar) do { unsigned _sp = 0; while (cond) { __builtin_amdgcn_s_sleep(1); \
;     if ((++_sp & 255u) == 0u) { if (xb_ld(&(bar)[XB_TMO])) break; if (_sp > XB_SPIN_CAP) { atomicAdd(&(bar)[XB_TMO], 1u); break; } } } } while (0)
; __device__ __forceinline__ void xcd_barrier(const XcdBarrier& b) {
;     ...
;         if (old + 1u == (gen + 1u) * nloc) {
;             __builtin_amdgcn_fence(__ATOMIC_RELEASE, "agent");
;             asm volatile("s_waitcnt vmcnt(0)" ::: "memory");
;             const unsigned og = xb_add(&bar[XB_TOP], 1u);
;             const unsigned tg = og / nx;
;             if (og + 1u == (tg + 1u) * nx) xb_add(&bar[XB_TOPGEN], 1u);
;             else XB_SPIN(xb_ld(&bar[XB_TOPGEN]) == tg, bar);
;             __builtin_amdgcn_fence(__ATOMIC_ACQUIRE, "agent");
.LBB0_184:
	s_andn2_saveexec_b64 s[4:5], s[4:5]
	s_cbranch_execz .LBB0_200
	v_mov_b32_e32 v1, s40
	v_add_co_u32_e32 v4, vcc, 0x3000, v1
	v_mov_b32_e32 v1, s41
	buffer_wbl2 sc1
	buffer_inv sc1
	s_waitcnt vmcnt(0)
	v_addc_co_u32_e32 v5, vcc, 0, v1, vcc
	flat_atomic_add v3, v[4:5], v238 offset:1024 sc0
	v_cvt_f32_u32_e32 v1, v2
	v_sub_u32_e32 v4, 0, v2
	s_mov_b64 s[8:9], -1
	v_rcp_iflag_f32_e32 v1, v1
	s_nop 0
	v_mul_f32_e32 v1, 0x4f7ffffe, v1
	v_cvt_u32_f32_e32 v1, v1
	v_mul_lo_u32 v4, v4, v1
	v_mul_hi_u32 v4, v1, v4
	v_add_u32_e32 v1, v1, v4
	s_waitcnt vmcnt(0) lgkmcnt(0)
	v_mul_hi_u32 v1, v3, v1
	v_mul_lo_u32 v4, v1, v2
	v_sub_u32_e32 v4, v3, v4
	v_cmp_ge_u32_e32 vcc, v4, v2
	v_add_u32_e32 v5, 1, v1
	s_nop 0
	v_cndmask_b32_e32 v1, v1, v5, vcc
	v_sub_u32_e32 v5, v4, v2
	v_cndmask_b32_e32 v4, v4, v5, vcc
	v_cmp_ge_u32_e32 vcc, v4, v2
	v_add_u32_e32 v4, 1, v1
	s_nop 0
	v_cndmask_b32_e32 v1, v1, v4, vcc
	v_add_u32_e32 v4, 1, v3
	v_mad_u64_u32 v[2:3], s[4:5], v2, v1, v[2:3]
	s_add_u32 s4, s40, 0x3500
	s_addc_u32 s5, s41, 0
	v_cmp_ne_u32_e32 vcc, v4, v2
	v_mov_b64_e32 v[2:3], s[4:5]
	s_and_saveexec_b64 s[6:7], vcc
	s_cbranch_execz .LBB0_197
	v_mov_b64_e32 v[2:3], s[4:5]
	flat_load_dword v2, v[2:3] sc1
	s_mov_b64 s[12:13], 0
	s_waitcnt vmcnt(0) lgkmcnt(0)
	v_cmp_eq_u32_e32 vcc, v2, v1
	s_and_saveexec_b64 s[10:11], vcc
	s_cbranch_execz .LBB0_196
	s_add_u32 s8, s40, 0x200
	s_addc_u32 s9, s41, 0
	s_mov_b32 s24, 1
	s_branch .LBB0_189

; __device__ __forceinline__ unsigned xb_add(unsigned* p, unsigned v) { return __hip_atomic_fetch_add(p, v, __ATOMIC_RELAXED, __HIP_MEMORY_SCOPE_AGENT); }
; __device__ __forceinline__ void xcd_barrier(const XcdBarrier& b) {
;     ...
;             __builtin_amdgcn_fence(__ATOMIC_ACQUIRE, "agent");
;             xb_add(&bar[XB_XGEN(bx)], 1u);
.LBB0_199:
	s_or_b64 exec, exec, s[4:5]
	s_add_i32 s66, s2, 0x900
	s_lshl_b64 s[4:5], s[66:67], 2
	s_add_u32 s4, s40, s4
	s_addc_u32 s5, s41, s5
	v_mov_b64_e32 v[2:3], s[4:5]
	s_waitcnt vmcnt(0) lgkmcnt(0)
	flat_atomic_add v[2:3], v238
	s_waitcnt vmcnt(0)

; __device__ __forceinline__ unsigned xb_ld(unsigned* p)              { return __hip_atomic_load(p, __ATOMIC_RELAXED, __HIP_MEMORY_SCOPE_AGENT); }
; __device__ __forceinline__ unsigned xb_add(unsigned* p, unsigned v) { return __hip_atomic_fetch_add(p, v, __ATOMIC_RELAXED, __HIP_MEMORY_SCOPE_AGENT); }
; #define XB_SPIN(cond, bar) do { unsigned _sp = 0; while (cond) { __builtin_amdgcn_s_sleep(1); \
;     if ((++_sp & 255u) == 0u) { if (xb_ld(&(bar)[XB_TMO])) break; if (_sp > XB_SPIN_CAP) { atomicAdd(&(bar)[XB_TMO], 1u); break; } } } } while (0)
; __device__ __forceinline__ void xcd_barrier(const XcdBarrier& b) {
;     ...
;         if (old + 1u == (gen + 1u) * nloc) {
;             __builtin_amdgcn_fence(__ATOMIC_RELEASE, "agent");
;             asm volatile("s_waitcnt vmcnt(0)" ::: "memory");
;             const unsigned og = xb_add(&bar[XB_TOP], 1u);
;             const unsigned tg = og / nx;
;             if (og + 1u == (tg + 1u) * nx) xb_add(&bar[XB_TOPGEN], 1u);
;             else XB_SPIN(xb_ld(&bar[XB_TOPGEN]) == tg, bar);
;             __builtin_amdgcn_fence(__ATOMIC_ACQUIRE, "agent");
.LBB0_756:
	s_andn2_saveexec_b64 s[4:5], s[4:5]
	s_cbranch_execz .LBB0_772
	v_mov_b32_e32 v1, s38
	v_add_co_u32_e32 v4, vcc, 0x3000, v1
	v_mov_b32_e32 v1, s39
	buffer_wbl2 sc1
	buffer_inv sc1
	s_waitcnt vmcnt(0)
	v_addc_co_u32_e32 v5, vcc, 0, v1, vcc
	flat_atomic_add v3, v[4:5], v238 offset:1024 sc0
	v_cvt_f32_u32_e32 v1, v2
	v_sub_u32_e32 v4, 0, v2
	s_mov_b64 s[8:9], -1
	v_rcp_iflag_f32_e32 v1, v1
	s_nop 0
	v_mul_f32_e32 v1, 0x4f7ffffe, v1
	v_cvt_u32_f32_e32 v1, v1
	v_mul_lo_u32 v4, v4, v1
	v_mul_hi_u32 v4, v1, v4
	v_add_u32_e32 v1, v1, v4
	s_waitcnt vmcnt(0) lgkmcnt(0)
	v_mul_hi_u32 v1, v3, v1
	v_mul_lo_u32 v4, v1, v2
	v_sub_u32_e32 v4, v3, v4
	v_cmp_ge_u32_e32 vcc, v4, v2
	v_add_u32_e32 v5, 1, v1
	s_nop 0
	v_cndmask_b32_e32 v1, v1, v5, vcc
	v_sub_u32_e32 v5, v4, v2
	v_cndmask_b32_e32 v4, v4, v5, vcc
	v_cmp_ge_u32_e32 vcc, v4, v2
	v_add_u32_e32 v4, 1, v1
	s_nop 0
	v_cndmask_b32_e32 v1, v1, v4, vcc
	v_add_u32_e32 v4, 1, v3
	v_mad_u64_u32 v[2:3], s[4:5], v2, v1, v[2:3]
	s_add_u32 s4, s38, 0x3500
	s_addc_u32 s5, s39, 0
	v_cmp_ne_u32_e32 vcc, v4, v2
	v_mov_b64_e32 v[2:3], s[4:5]
	s_and_saveexec_b64 s[6:7], vcc
	s_cbranch_execz .LBB0_769
	v_mov_b64_e32 v[2:3], s[4:5]
	flat_load_dword v2, v[2:3] sc1
	s_mov_b64 s[12:13], 0
	s_waitcnt vmcnt(0) lgkmcnt(0)
	v_cmp_eq_u32_e32 vcc, v2, v1
	s_and_saveexec_b64 s[10:11], vcc
	s_cbranch_execz .LBB0_768
	s_add_u32 s8, s38, 0x200
	s_addc_u32 s9, s39, 0
	s_mov_b32 s24, 1
	s_branch .LBB0_761

; __device__ __forceinline__ unsigned xb_ld(unsigned* p)              { return __hip_atomic_load(p, __ATOMIC_RELAXED, __HIP_MEMORY_SCOPE_AGENT); }
; __device__ __forceinline__ unsigned xb_add(unsigned* p, unsigned v) { return __hip_atomic_fetch_add(p, v, __ATOMIC_RELAXED, __HIP_MEMORY_SCOPE_AGENT); }
; #define XB_SPIN(cond, bar) do { unsigned _sp = 0; while (cond) { __builtin_amdgcn_s_sleep(1); \
;     if ((++_sp & 255u) == 0u) { if (xb_ld(&(bar)[XB_TMO])) break; if (_sp > XB_SPIN_CAP) { atomicAdd(&(bar)[XB_TMO], 1u); break; } } } } while (0)
; __device__ __forceinline__ void xcd_barrier(const XcdBarrier& b) {
;     ...
;         if (old + 1u == (gen + 1u) * nloc) {
;             __builtin_amdgcn_fence(__ATOMIC_RELEASE, "agent");
;             asm volatile("s_waitcnt vmcnt(0)" ::: "memory");
;             const unsigned og = xb_add(&bar[XB_TOP], 1u);
;             const unsigned tg = og / nx;
;             if (og + 1u == (tg + 1u) * nx) xb_add(&bar[XB_TOPGEN], 1u);
;             else XB_SPIN(xb_ld(&bar[XB_TOPGEN]) == tg, bar);
;             __builtin_amdgcn_fence(__ATOMIC_ACQUIRE, "agent");
.LBB0_1350:
	v_mov_b32_e32 v1, s38
	v_add_co_u32_e32 v4, vcc, 0x3000, v1
	v_mov_b32_e32 v1, s39
	buffer_wbl2 sc1
	buffer_inv sc1
	s_waitcnt vmcnt(0)
	v_addc_co_u32_e32 v5, vcc, 0, v1, vcc
	flat_atomic_add v3, v[4:5], v238 offset:1024 sc0
	v_cvt_f32_u32_e32 v1, v2
	v_sub_u32_e32 v4, 0, v2
	s_mov_b64 s[8:9], -1
	v_rcp_iflag_f32_e32 v1, v1
	s_nop 0
	v_mul_f32_e32 v1, 0x4f7ffffe, v1
	v_cvt_u32_f32_e32 v1, v1
	v_mul_lo_u32 v4, v4, v1
	v_mul_hi_u32 v4, v1, v4
	v_add_u32_e32 v1, v1, v4
	s_waitcnt vmcnt(0) lgkmcnt(0)
	v_mul_hi_u32 v1, v3, v1
	v_mul_lo_u32 v4, v1, v2
	v_sub_u32_e32 v4, v3, v4
	v_cmp_ge_u32_e32 vcc, v4, v2
	v_add_u32_e32 v5, 1, v1
	s_nop 0
	v_cndmask_b32_e32 v1, v1, v5, vcc
	v_sub_u32_e32 v5, v4, v2
	v_cndmask_b32_e32 v4, v4, v5, vcc
	v_cmp_ge_u32_e32 vcc, v4, v2
	v_add_u32_e32 v4, 1, v1
	s_nop 0
	v_cndmask_b32_e32 v1, v1, v4, vcc
	v_add_u32_e32 v4, 1, v3
	v_mad_u64_u32 v[2:3], s[4:5], v2, v1, v[2:3]
	s_add_u32 s4, s38, 0x3500
	s_addc_u32 s5, s39, 0
	v_cmp_ne_u32_e32 vcc, v4, v2
	v_mov_b64_e32 v[2:3], s[4:5]
	s_and_saveexec_b64 s[6:7], vcc
	s_cbranch_execz .LBB0_1362
	v_mov_b64_e32 v[2:3], s[4:5]
	flat_load_dword v2, v[2:3] sc1
	s_mov_b64 s[12:13], 0
	s_waitcnt vmcnt(0) lgkmcnt(0)
	v_cmp_eq_u32_e32 vcc, v2, v1
	s_and_saveexec_b64 s[10:11], vcc
	s_cbranch_execz .LBB0_1361
	s_add_u32 s8, s38, 0x200
	s_addc_u32 s9, s39, 0
	s_mov_b32 s24, 1
	s_branch .LBB0_1354
